# dilated-attention passes 1 and 2: epilogue rows staged through the wave's LDS tile buffer, 8 global_store_dwordx4 instead of 32 global_store_dword per item
# baseline (speedup 1.0000x reference)
; __device__ __forceinline__ float lane_xor1(float v) { return dpp_f<0xB1>(v); }
; __device__ __forceinline__ int crow(int r, int hi) { return (r & 3) + 8 * (r >> 2) + 4 * hi; }
; __device__ __forceinline__ unsigned cvtpk(float lo, float hi) { unsigned r; asm volatile("v_cvt_pk_bf16_f32 %0, %1, %2" : "=v"(r) : "v"(lo), "v"(hi)); return r; }
; __device__ __forceinline__ void store_o_bf16(const f32x16* o, const float* rli, bf16* Ow, int ldo, int lane, int r32, int hi) {
;   const unsigned loff = (unsigned)((((lane & 1) + 4 * hi) * ldo + (r32 & ~1)) * 2);
; #pragma unroll
;   for (int r = 0; r < 16; r += 2) {
;     char* rowp = (char*)(Ow + (size_t)((r & 3) + 8 * (r >> 2)) * ldo);
; #pragma unroll
;     for (int d0 = 0; d0 < 4; ++d0) {
;       const float a = o[d0][r] * rli[r], b = o[d0][r + 1] * rli[r + 1];
;       const float send = (lane & 1) ? a : b; const float recv = lane_xor1(send);
;       const unsigned w = cvtpk((lane & 1) ? recv : a, (lane & 1) ? b : recv);
;       *(unsigned*)(rowp + loff + d0 * 64) = w; } }
; }
; template <int PASS>
; __device__ __forceinline__ void attn_a_pass(LAS unsigned char* lds_all, const bf16* ZA, bf16* Oabc, float* ML, const float* rel_bias, int gw, int ngw, int xcd, int inx, int tid) {
;     ...
;         if (hf == 0) li_l[r32] = l_reg;
;         asm volatile("s_waitcnt lgkmcnt(0)" ::: "memory");
;         float rli[16];
; #pragma unroll
;         for (int r = 0; r < 16; ++r) rli[r] = __builtin_amdgcn_rcpf(li_l[crow(r, hf)]);
;         store_o_bf16(o, rli, Ob, RSTR * 3072, lane, r32, hf);
.LBB0_947:
	s_and_saveexec_b64 s[6:7], s[4:5]
	ds_write_b32 v202, v195
	s_or_b64 exec, exec, s[6:7]
	s_waitcnt lgkmcnt(0)
	ds_read_b128 v[66:69], v198
	ds_read_b128 v[70:73], v198 offset:32
	s_lshl_b64 s[14:15], s[14:15], 12
	s_waitcnt vmcnt(15)
	v_and_b32_e32 v84, 1, v191
	s_or_b32 s14, s14, s68
	s_waitcnt lgkmcnt(1)
	v_rcp_f32_e32 v74, v66
	v_rcp_f32_e32 v75, v67
	v_cmp_eq_u32_e32 vcc, 0, v84
	s_mul_i32 s6, s15, 0x1800
	v_mul_f32_e32 v50, v50, v74
	v_mul_f32_e32 v51, v51, v75
	s_mul_hi_u32 s7, s14, 0x1800
	v_or_b32_e32 v0, v196, v84
	v_cndmask_b32_e32 v84, v50, v51, vcc
	s_add_i32 s7, s7, s6
	s_mul_i32 s6, s14, 0x1800
	v_mul_lo_u32 v0, v0, s92
	v_mov_b32_dpp v84, v84 quad_perm:[1,0,3,2] row_mask:0xf bank_mask:0xf bound_ctrl:1
	s_add_u32 s6, s31, s6
	v_and_or_b32 v0, v191, 30, v0
	v_cndmask_b32_e32 v50, v84, v50, vcc
	s_addc_u32 s7, s34, s7
	v_rcp_f32_e32 v76, v68
	v_rcp_f32_e32 v77, v69
	s_waitcnt lgkmcnt(0)
	v_rcp_f32_e32 v78, v70
	ds_read_b128 v[66:69], v198 offset:64
	v_rcp_f32_e32 v79, v71
	v_rcp_f32_e32 v80, v72
	v_rcp_f32_e32 v81, v73
	ds_read_b128 v[70:73], v198 offset:96
	v_lshlrev_b32_e32 v0, 1, v0
	v_cndmask_b32_e32 v51, v51, v84, vcc
	v_cvt_pk_bf16_f32 v50, v50, v51
	v_mul_f32_e32 v34, v34, v74
	v_mul_f32_e32 v35, v35, v75
	v_lshrrev_b32_e32 v100, 4, v191
	v_mul_u32_u24_e32 v100, 0x1800, v100
	v_and_b32_e32 v101, 15, v191
	v_lshl_add_u32 v100, v101, 4, v100
	v_mov_b32_e32 v101, 0
	v_lshl_add_u64 v[100:101], s[6:7], 0, v[100:101]
	v_and_b32_e32 v98, 1, v191
	v_lshrrev_b32_e32 v99, 3, v191
	v_and_b32_e32 v99, 4, v99
	v_add_u32_e32 v98, v98, v99
	v_lshlrev_b32_e32 v98, 8, v98
	v_and_b32_e32 v99, 30, v191
	v_lshl_add_u32 v98, v99, 1, v98
	v_add_u32_e32 v98, s25, v98
	v_lshlrev_b32_e32 v99, 4, v191
	v_add_u32_e32 v99, s25, v99
	ds_write_b32 v98, v50 offset:0
	v_cndmask_b32_e32 v50, v34, v35, vcc
	v_mul_f32_e32 v18, v18, v74
	v_mul_f32_e32 v19, v19, v75
	v_mov_b32_dpp v50, v50 quad_perm:[1,0,3,2] row_mask:0xf bank_mask:0xf bound_ctrl:1
	v_cndmask_b32_e32 v34, v50, v34, vcc
	v_cndmask_b32_e32 v35, v35, v50, vcc
	v_cvt_pk_bf16_f32 v34, v34, v35
	ds_write_b32 v98, v34 offset:64
	v_cndmask_b32_e32 v34, v18, v19, vcc
	v_mul_f32_e32 v2, v2, v74
	v_mul_f32_e32 v3, v3, v75
	v_mov_b32_dpp v34, v34 quad_perm:[1,0,3,2] row_mask:0xf bank_mask:0xf bound_ctrl:1
	v_cndmask_b32_e32 v18, v34, v18, vcc
	v_cndmask_b32_e32 v19, v19, v34, vcc
	v_cvt_pk_bf16_f32 v18, v18, v19
	ds_write_b32 v98, v18 offset:128
	v_cndmask_b32_e32 v18, v2, v3, vcc
	s_waitcnt lgkmcnt(1)
	v_rcp_f32_e32 v82, v66
	v_rcp_f32_e32 v83, v67
	v_mov_b32_dpp v18, v18 quad_perm:[1,0,3,2] row_mask:0xf bank_mask:0xf bound_ctrl:1
	v_cndmask_b32_e32 v2, v18, v2, vcc
	v_cndmask_b32_e32 v3, v3, v18, vcc
	v_cvt_pk_bf16_f32 v2, v2, v3
	v_lshl_add_u64 v[66:67], s[6:7], 0, v[0:1]
	ds_write_b32 v98, v2 offset:192
	v_mul_f32_e32 v0, v52, v76
	v_mul_f32_e32 v2, v53, v77
	v_cndmask_b32_e32 v3, v0, v2, vcc
	v_mul_f32_e32 v18, v37, v77
	v_rcp_f32_e32 v68, v68
	v_mov_b32_dpp v3, v3 quad_perm:[1,0,3,2] row_mask:0xf bank_mask:0xf bound_ctrl:1
	v_cndmask_b32_e32 v0, v3, v0, vcc
	v_cndmask_b32_e32 v2, v2, v3, vcc
	v_cvt_pk_bf16_f32 v0, v0, v2
	v_add_co_u32_e64 v2, s[6:7], s37, v66
	v_rcp_f32_e32 v69, v69
	s_nop 0
	v_addc_co_u32_e64 v3, s[6:7], 0, v67, s[6:7]
	ds_write_b32 v98, v0 offset:512
	v_mul_f32_e32 v0, v36, v76
	v_cndmask_b32_e32 v19, v0, v18, vcc
	s_waitcnt lgkmcnt(0)
	v_rcp_f32_e32 v70, v70
	v_rcp_f32_e32 v71, v71
	v_mov_b32_dpp v19, v19 quad_perm:[1,0,3,2] row_mask:0xf bank_mask:0xf bound_ctrl:1
	v_cndmask_b32_e32 v0, v19, v0, vcc
	v_cndmask_b32_e32 v18, v18, v19, vcc
	v_cvt_pk_bf16_f32 v0, v0, v18
	ds_write_b32 v98, v0 offset:576
	v_mul_f32_e32 v0, v20, v76
	v_mul_f32_e32 v18, v21, v77
	v_cndmask_b32_e32 v19, v0, v18, vcc
	v_rcp_f32_e32 v72, v72
	v_rcp_f32_e32 v73, v73
	v_mov_b32_dpp v19, v19 quad_perm:[1,0,3,2] row_mask:0xf bank_mask:0xf bound_ctrl:1
	v_cndmask_b32_e32 v0, v19, v0, vcc
	v_cndmask_b32_e32 v18, v18, v19, vcc
	v_cvt_pk_bf16_f32 v0, v0, v18
	ds_write_b32 v98, v0 offset:640
	v_mul_f32_e32 v0, v4, v76
	v_mul_f32_e32 v4, v5, v77
	v_cndmask_b32_e32 v5, v0, v4, vcc
	s_nop 1
	v_mov_b32_dpp v5, v5 quad_perm:[1,0,3,2] row_mask:0xf bank_mask:0xf bound_ctrl:1
	v_cndmask_b32_e32 v0, v5, v0, vcc
	v_cndmask_b32_e32 v4, v4, v5, vcc
	v_cvt_pk_bf16_f32 v0, v0, v4
	ds_write_b32 v98, v0 offset:704
	v_mul_f32_e32 v0, v54, v78
	v_mul_f32_e32 v2, v55, v79
	v_cndmask_b32_e32 v3, v0, v2, vcc
	v_mul_f32_e32 v4, v39, v79
	s_nop 0
	v_mov_b32_dpp v3, v3 quad_perm:[1,0,3,2] row_mask:0xf bank_mask:0xf bound_ctrl:1
	v_cndmask_b32_e32 v0, v3, v0, vcc
	v_cndmask_b32_e32 v2, v2, v3, vcc
	v_cvt_pk_bf16_f32 v0, v0, v2
	v_add_co_u32_e64 v2, s[6:7], s70, v66
	s_nop 1
	v_addc_co_u32_e64 v3, s[6:7], 0, v67, s[6:7]
	ds_write_b32 v98, v0 offset:2048
	v_mul_f32_e32 v0, v38, v78
	v_cndmask_b32_e32 v5, v0, v4, vcc
	s_mov_b32 s6, 0xf000
	s_nop 0
	v_mov_b32_dpp v5, v5 quad_perm:[1,0,3,2] row_mask:0xf bank_mask:0xf bound_ctrl:1
	v_cndmask_b32_e32 v0, v5, v0, vcc
	v_cndmask_b32_e32 v4, v4, v5, vcc
	v_cvt_pk_bf16_f32 v0, v0, v4
	ds_write_b32 v98, v0 offset:2112
	v_mul_f32_e32 v0, v22, v78
	v_mul_f32_e32 v4, v23, v79
	v_cndmask_b32_e32 v5, v0, v4, vcc
	s_nop 1
	v_mov_b32_dpp v5, v5 quad_perm:[1,0,3,2] row_mask:0xf bank_mask:0xf bound_ctrl:1
	v_cndmask_b32_e32 v0, v5, v0, vcc
	v_cndmask_b32_e32 v4, v4, v5, vcc
	v_cvt_pk_bf16_f32 v0, v0, v4
	ds_write_b32 v98, v0 offset:2176
	v_mul_f32_e32 v0, v6, v78
	v_mul_f32_e32 v4, v7, v79
	v_cndmask_b32_e32 v5, v0, v4, vcc
	s_nop 1
	v_mov_b32_dpp v5, v5 quad_perm:[1,0,3,2] row_mask:0xf bank_mask:0xf bound_ctrl:1
	v_cndmask_b32_e32 v0, v5, v0, vcc
	v_cndmask_b32_e32 v4, v4, v5, vcc
; __device__ __forceinline__ float lane_xor1(float v) { return dpp_f<0xB1>(v); }
; __device__ __forceinline__ unsigned cvtpk(float lo, float hi) { unsigned r; asm volatile("v_cvt_pk_bf16_f32 %0, %1, %2" : "=v"(r) : "v"(lo), "v"(hi)); return r; }
; __device__ __forceinline__ void store_o_bf16(const f32x16* o, const float* rli, bf16* Ow, int ldo, int lane, int r32, int hi) {
;     ...
;   for (int r = 0; r < 16; r += 2) {
;     char* rowp = (char*)(Ow + (size_t)((r & 3) + 8 * (r >> 2)) * ldo);
; #pragma unroll
;     for (int d0 = 0; d0 < 4; ++d0) {
;       const float a = o[d0][r] * rli[r], b = o[d0][r + 1] * rli[r + 1];
;       const float send = (lane & 1) ? a : b; const float recv = lane_xor1(send);
;       const unsigned w = cvtpk((lane & 1) ? recv : a, (lane & 1) ? b : recv);
;       *(unsigned*)(rowp + loff + d0 * 64) = w; } }
	v_cvt_pk_bf16_f32 v0, v0, v4
	ds_write_b32 v98, v0 offset:2240
	v_mul_f32_e32 v0, v56, v80
	v_mul_f32_e32 v2, v57, v81
	v_cndmask_b32_e32 v3, v0, v2, vcc
	v_mul_f32_e32 v4, v41, v81
	s_nop 0
	v_mov_b32_dpp v3, v3 quad_perm:[1,0,3,2] row_mask:0xf bank_mask:0xf bound_ctrl:1
	v_cndmask_b32_e32 v0, v3, v0, vcc
	v_cndmask_b32_e32 v2, v2, v3, vcc
	v_cvt_pk_bf16_f32 v0, v0, v2
	v_add_co_u32_e64 v2, s[6:7], s6, v66
	s_nop 1
	v_addc_co_u32_e64 v3, s[6:7], 0, v67, s[6:7]
	ds_write_b32 v98, v0 offset:2560
	v_mul_f32_e32 v0, v40, v80
	v_cndmask_b32_e32 v5, v0, v4, vcc
	s_nop 1
	v_mov_b32_dpp v5, v5 quad_perm:[1,0,3,2] row_mask:0xf bank_mask:0xf bound_ctrl:1
	v_cndmask_b32_e32 v0, v5, v0, vcc
	v_cndmask_b32_e32 v4, v4, v5, vcc
	v_cvt_pk_bf16_f32 v0, v0, v4
	ds_write_b32 v98, v0 offset:2624
	v_mul_f32_e32 v0, v24, v80
	v_mul_f32_e32 v4, v25, v81
	v_cndmask_b32_e32 v5, v0, v4, vcc
	s_nop 1
	v_mov_b32_dpp v5, v5 quad_perm:[1,0,3,2] row_mask:0xf bank_mask:0xf bound_ctrl:1
	v_cndmask_b32_e32 v0, v5, v0, vcc
	v_cndmask_b32_e32 v4, v4, v5, vcc
	v_cvt_pk_bf16_f32 v0, v0, v4
	ds_write_b32 v98, v0 offset:2688
	v_mul_f32_e32 v0, v8, v80
	v_mul_f32_e32 v4, v9, v81
	v_cndmask_b32_e32 v5, v0, v4, vcc
	s_nop 1
	v_mov_b32_dpp v5, v5 quad_perm:[1,0,3,2] row_mask:0xf bank_mask:0xf bound_ctrl:1
	v_cndmask_b32_e32 v0, v5, v0, vcc
	v_cndmask_b32_e32 v4, v4, v5, vcc
	v_cvt_pk_bf16_f32 v0, v0, v4
	ds_write_b32 v98, v0 offset:2752
	v_mul_f32_e32 v0, v58, v82
	v_mul_f32_e32 v2, v59, v83
	v_cndmask_b32_e32 v3, v0, v2, vcc
	v_mul_f32_e32 v4, v43, v83
	s_nop 0
	v_mov_b32_dpp v3, v3 quad_perm:[1,0,3,2] row_mask:0xf bank_mask:0xf bound_ctrl:1
	v_cndmask_b32_e32 v0, v3, v0, vcc
	v_cndmask_b32_e32 v2, v2, v3, vcc
	v_cvt_pk_bf16_f32 v0, v0, v2
	v_add_co_u32_e64 v2, s[6:7], s93, v66
	s_nop 1
	v_addc_co_u32_e64 v3, s[6:7], 0, v67, s[6:7]
	ds_write_b32 v98, v0 offset:4096
	v_mul_f32_e32 v0, v42, v82
	v_cndmask_b32_e32 v5, v0, v4, vcc
	s_mov_b32 s6, 0x1b000
	s_nop 0
	v_mov_b32_dpp v5, v5 quad_perm:[1,0,3,2] row_mask:0xf bank_mask:0xf bound_ctrl:1
	v_cndmask_b32_e32 v0, v5, v0, vcc
	v_cndmask_b32_e32 v4, v4, v5, vcc
	v_cvt_pk_bf16_f32 v0, v0, v4
	ds_write_b32 v98, v0 offset:4160
	v_mul_f32_e32 v0, v26, v82
	v_mul_f32_e32 v4, v27, v83
	v_cndmask_b32_e32 v5, v0, v4, vcc
	s_nop 1
	v_mov_b32_dpp v5, v5 quad_perm:[1,0,3,2] row_mask:0xf bank_mask:0xf bound_ctrl:1
	v_cndmask_b32_e32 v0, v5, v0, vcc
	v_cndmask_b32_e32 v4, v4, v5, vcc
	v_cvt_pk_bf16_f32 v0, v0, v4
	ds_write_b32 v98, v0 offset:4224
	v_mul_f32_e32 v0, v10, v82
	v_mul_f32_e32 v4, v11, v83
	v_cndmask_b32_e32 v5, v0, v4, vcc
	s_nop 1
	v_mov_b32_dpp v5, v5 quad_perm:[1,0,3,2] row_mask:0xf bank_mask:0xf bound_ctrl:1
	v_cndmask_b32_e32 v0, v5, v0, vcc
	v_cndmask_b32_e32 v4, v4, v5, vcc
	v_cvt_pk_bf16_f32 v0, v0, v4
	ds_write_b32 v98, v0 offset:4288
	v_mul_f32_e32 v0, v60, v68
	v_mul_f32_e32 v2, v61, v69
	v_cndmask_b32_e32 v3, v0, v2, vcc
	v_mul_f32_e32 v4, v45, v69
	s_nop 0
	v_mov_b32_dpp v3, v3 quad_perm:[1,0,3,2] row_mask:0xf bank_mask:0xf bound_ctrl:1
	v_cndmask_b32_e32 v0, v3, v0, vcc
	v_cndmask_b32_e32 v2, v2, v3, vcc
	v_cvt_pk_bf16_f32 v0, v0, v2
	v_add_co_u32_e64 v2, s[6:7], s6, v66
	s_nop 1
	v_addc_co_u32_e64 v3, s[6:7], 0, v67, s[6:7]
	ds_write_b32 v98, v0 offset:4608
	v_mul_f32_e32 v0, v44, v68
	v_cndmask_b32_e32 v5, v0, v4, vcc
	s_mov_b32 s6, 0x24000
	s_nop 0
	v_mov_b32_dpp v5, v5 quad_perm:[1,0,3,2] row_mask:0xf bank_mask:0xf bound_ctrl:1
	v_cndmask_b32_e32 v0, v5, v0, vcc
	v_cndmask_b32_e32 v4, v4, v5, vcc
	v_cvt_pk_bf16_f32 v0, v0, v4
	ds_write_b32 v98, v0 offset:4672
	v_mul_f32_e32 v0, v28, v68
	v_mul_f32_e32 v4, v29, v69
	v_cndmask_b32_e32 v5, v0, v4, vcc
	s_nop 1
	v_mov_b32_dpp v5, v5 quad_perm:[1,0,3,2] row_mask:0xf bank_mask:0xf bound_ctrl:1
	v_cndmask_b32_e32 v0, v5, v0, vcc
	v_cndmask_b32_e32 v4, v4, v5, vcc
	v_cvt_pk_bf16_f32 v0, v0, v4
	ds_write_b32 v98, v0 offset:4736
	v_mul_f32_e32 v0, v12, v68
	v_mul_f32_e32 v4, v13, v69
	v_cndmask_b32_e32 v5, v0, v4, vcc
	s_nop 1
	v_mov_b32_dpp v5, v5 quad_perm:[1,0,3,2] row_mask:0xf bank_mask:0xf bound_ctrl:1
	v_cndmask_b32_e32 v0, v5, v0, vcc
	v_cndmask_b32_e32 v4, v4, v5, vcc
	v_cvt_pk_bf16_f32 v0, v0, v4
	ds_write_b32 v98, v0 offset:4800
	v_mul_f32_e32 v0, v62, v70
	v_mul_f32_e32 v2, v63, v71
	v_cndmask_b32_e32 v3, v0, v2, vcc
	v_mul_f32_e32 v4, v47, v71
	s_nop 0
	v_mov_b32_dpp v3, v3 quad_perm:[1,0,3,2] row_mask:0xf bank_mask:0xf bound_ctrl:1
	v_cndmask_b32_e32 v0, v3, v0, vcc
	v_cndmask_b32_e32 v2, v2, v3, vcc
	v_cvt_pk_bf16_f32 v0, v0, v2
	v_add_co_u32_e64 v2, s[6:7], s6, v66
; __device__ __forceinline__ float lane_xor1(float v) { return dpp_f<0xB1>(v); }
; __device__ __forceinline__ unsigned cvtpk(float lo, float hi) { unsigned r; asm volatile("v_cvt_pk_bf16_f32 %0, %1, %2" : "=v"(r) : "v"(lo), "v"(hi)); return r; }
; __device__ __forceinline__ void store_o_bf16(const f32x16* o, const float* rli, bf16* Ow, int ldo, int lane, int r32, int hi) {
;     ...
;   for (int r = 0; r < 16; r += 2) {
;     char* rowp = (char*)(Ow + (size_t)((r & 3) + 8 * (r >> 2)) * ldo);
; #pragma unroll
;     for (int d0 = 0; d0 < 4; ++d0) {
;       const float a = o[d0][r] * rli[r], b = o[d0][r + 1] * rli[r + 1];
;       const float send = (lane & 1) ? a : b; const float recv = lane_xor1(send);
;       const unsigned w = cvtpk((lane & 1) ? recv : a, (lane & 1) ? b : recv);
;       *(unsigned*)(rowp + loff + d0 * 64) = w; } }
; template <int PASS>
; __device__ __forceinline__ void attn_a_pass(LAS unsigned char* lds_all, const bf16* ZA, bf16* Oabc, float* ML, const float* rel_bias, int gw, int ngw, int xcd, int inx, int tid) {
;     ...
;         store_o_bf16(o, rli, Ob, RSTR * 3072, lane, r32, hf);
;         if (PASS == 1 && hf == 0) *(float2*)(MLb + (size_t)r32 * 16) = make_float2(m_reg, l_reg);
	s_nop 1
	v_addc_co_u32_e64 v3, s[6:7], 0, v67, s[6:7]
	ds_write_b32 v98, v0 offset:6144
	v_mul_f32_e32 v0, v46, v70
	v_cndmask_b32_e32 v5, v0, v4, vcc
	s_mov_b32 s6, 0x27000
	s_nop 0
	v_mov_b32_dpp v5, v5 quad_perm:[1,0,3,2] row_mask:0xf bank_mask:0xf bound_ctrl:1
	v_cndmask_b32_e32 v0, v5, v0, vcc
	v_cndmask_b32_e32 v4, v4, v5, vcc
	v_cvt_pk_bf16_f32 v0, v0, v4
	ds_write_b32 v98, v0 offset:6208
	v_mul_f32_e32 v0, v30, v70
	v_mul_f32_e32 v4, v31, v71
	v_cndmask_b32_e32 v5, v0, v4, vcc
	s_nop 1
	v_mov_b32_dpp v5, v5 quad_perm:[1,0,3,2] row_mask:0xf bank_mask:0xf bound_ctrl:1
	v_cndmask_b32_e32 v0, v5, v0, vcc
	v_cndmask_b32_e32 v4, v4, v5, vcc
	v_cvt_pk_bf16_f32 v0, v0, v4
	ds_write_b32 v98, v0 offset:6272
	v_mul_f32_e32 v0, v14, v70
	v_mul_f32_e32 v4, v15, v71
	v_cndmask_b32_e32 v5, v0, v4, vcc
	s_nop 1
	v_mov_b32_dpp v5, v5 quad_perm:[1,0,3,2] row_mask:0xf bank_mask:0xf bound_ctrl:1
	v_cndmask_b32_e32 v0, v5, v0, vcc
	v_cndmask_b32_e32 v4, v4, v5, vcc
	v_cvt_pk_bf16_f32 v0, v0, v4
	ds_write_b32 v98, v0 offset:6336
	v_mul_f32_e32 v0, v64, v72
	v_mul_f32_e32 v2, v65, v73
	v_cndmask_b32_e32 v3, v0, v2, vcc
	v_mul_f32_e32 v4, v49, v73
	s_nop 0
	v_mov_b32_dpp v3, v3 quad_perm:[1,0,3,2] row_mask:0xf bank_mask:0xf bound_ctrl:1
	v_cndmask_b32_e32 v0, v3, v0, vcc
	v_cndmask_b32_e32 v2, v2, v3, vcc
	v_cvt_pk_bf16_f32 v0, v0, v2
	v_add_co_u32_e64 v2, s[6:7], s6, v66
	s_nop 1
	v_addc_co_u32_e64 v3, s[6:7], 0, v67, s[6:7]
	ds_write_b32 v98, v0 offset:6656
	v_mul_f32_e32 v0, v48, v72
	v_cndmask_b32_e32 v5, v0, v4, vcc
	s_nop 1
	v_mov_b32_dpp v5, v5 quad_perm:[1,0,3,2] row_mask:0xf bank_mask:0xf bound_ctrl:1
	v_cndmask_b32_e32 v0, v5, v0, vcc
	v_cndmask_b32_e32 v4, v4, v5, vcc
	v_cvt_pk_bf16_f32 v0, v0, v4
	ds_write_b32 v98, v0 offset:6720
	v_mul_f32_e32 v0, v32, v72
	v_mul_f32_e32 v4, v33, v73
	v_cndmask_b32_e32 v5, v0, v4, vcc
	s_nop 1
	v_mov_b32_dpp v5, v5 quad_perm:[1,0,3,2] row_mask:0xf bank_mask:0xf bound_ctrl:1
	v_cndmask_b32_e32 v0, v5, v0, vcc
	v_cndmask_b32_e32 v4, v4, v5, vcc
	v_cvt_pk_bf16_f32 v0, v0, v4
	ds_write_b32 v98, v0 offset:6784
	v_mul_f32_e32 v0, v16, v72
	v_mul_f32_e32 v4, v17, v73
	v_cndmask_b32_e32 v5, v0, v4, vcc
	s_nop 1
	v_mov_b32_dpp v5, v5 quad_perm:[1,0,3,2] row_mask:0xf bank_mask:0xf bound_ctrl:1
	v_cndmask_b32_e32 v0, v5, v0, vcc
	v_cndmask_b32_e32 v4, v4, v5, vcc
	v_cvt_pk_bf16_f32 v0, v0, v4
	ds_write_b32 v98, v0 offset:6848
	ds_read_b128 v[236:239], v99 offset:0
	ds_read_b128 v[240:243], v99 offset:1024
	ds_read_b128 v[244:247], v99 offset:2048
	ds_read_b128 v[248:251], v99 offset:3072
	s_waitcnt lgkmcnt(3)
	global_store_dwordx4 v[100:101], v[236:239], off
	s_mov_b32 s94, 0x6000
	v_add_co_u32_e64 v102, s[98:99], s94, v100
	s_nop 1
	v_addc_co_u32_e64 v103, s[98:99], 0, v101, s[98:99]
	s_waitcnt lgkmcnt(2)
	global_store_dwordx4 v[102:103], v[240:243], off
	s_mov_b32 s94, 0xc000
	v_add_co_u32_e64 v104, s[98:99], s94, v100
	s_nop 1
	v_addc_co_u32_e64 v105, s[98:99], 0, v101, s[98:99]
	s_waitcnt lgkmcnt(1)
	global_store_dwordx4 v[104:105], v[244:247], off
	s_mov_b32 s94, 0x12000
	v_add_co_u32_e64 v102, s[98:99], s94, v100
	s_nop 1
	v_addc_co_u32_e64 v103, s[98:99], 0, v101, s[98:99]
	s_waitcnt lgkmcnt(0)
	global_store_dwordx4 v[102:103], v[248:251], off
	ds_read_b128 v[204:207], v99 offset:4096
	ds_read_b128 v[208:211], v99 offset:5120
	ds_read_b128 v[212:215], v99 offset:6144
	ds_read_b128 v[110:113], v99 offset:7168
	s_mov_b32 s94, 0x18000
	v_add_co_u32_e64 v104, s[98:99], s94, v100
	s_nop 1
	v_addc_co_u32_e64 v105, s[98:99], 0, v101, s[98:99]
	s_waitcnt lgkmcnt(3)
	global_store_dwordx4 v[104:105], v[204:207], off
	s_mov_b32 s94, 0x1e000
	v_add_co_u32_e64 v102, s[98:99], s94, v100
	s_nop 1
	v_addc_co_u32_e64 v103, s[98:99], 0, v101, s[98:99]
	s_waitcnt lgkmcnt(2)
	global_store_dwordx4 v[102:103], v[208:211], off
	s_mov_b32 s94, 0x24000
	v_add_co_u32_e64 v104, s[98:99], s94, v100
	s_nop 1
	v_addc_co_u32_e64 v105, s[98:99], 0, v101, s[98:99]
	s_waitcnt lgkmcnt(1)
	global_store_dwordx4 v[104:105], v[212:215], off
	s_mov_b32 s94, 0x2a000
	v_add_co_u32_e64 v102, s[98:99], s94, v100
	s_nop 1
	v_addc_co_u32_e64 v103, s[98:99], 0, v101, s[98:99]
	s_waitcnt lgkmcnt(0)
	global_store_dwordx4 v[102:103], v[110:113], off
	s_and_saveexec_b64 s[6:7], s[4:5]
	s_mov_b32 s82, s80
	s_cbranch_execz .LBB0_935
	s_lshl_b64 s[4:5], s[14:15], 6
	s_add_u32 s4, s35, s4
	s_addc_u32 s5, s38, s5
	v_mov_b32_e32 v191, v1
	v_lshl_add_u64 v[2:3], v[190:191], 2, s[4:5]
	global_store_dwordx2 v[2:3], v[194:195], off
	s_branch .LBB0_935

; __device__ __forceinline__ float lane_xor1(float v) { return dpp_f<0xB1>(v); }
; __device__ __forceinline__ int crow(int r, int hi) { return (r & 3) + 8 * (r >> 2) + 4 * hi; }
; __device__ __forceinline__ unsigned cvtpk(float lo, float hi) { unsigned r; asm volatile("v_cvt_pk_bf16_f32 %0, %1, %2" : "=v"(r) : "v"(lo), "v"(hi)); return r; }
; __device__ __forceinline__ void store_o_bf16(const f32x16* o, const float* rli, bf16* Ow, int ldo, int lane, int r32, int hi) {
;   const unsigned loff = (unsigned)((((lane & 1) + 4 * hi) * ldo + (r32 & ~1)) * 2);
; #pragma unroll
;   for (int r = 0; r < 16; r += 2) {
;     char* rowp = (char*)(Ow + (size_t)((r & 3) + 8 * (r >> 2)) * ldo);
; #pragma unroll
;     for (int d0 = 0; d0 < 4; ++d0) {
;       const float a = o[d0][r] * rli[r], b = o[d0][r + 1] * rli[r + 1];
;       const float send = (lane & 1) ? a : b; const float recv = lane_xor1(send);
;       const unsigned w = cvtpk((lane & 1) ? recv : a, (lane & 1) ? b : recv);
;       *(unsigned*)(rowp + loff + d0 * 64) = w; } }
; }
; template <int PASS>
; __device__ __forceinline__ void attn_a_pass(LAS unsigned char* lds_all, const bf16* ZA, bf16* Oabc, float* ML, const float* rel_bias, int gw, int ngw, int xcd, int inx, int tid) {
;     ...
;         if (hf == 0) li_l[r32] = l_reg;
;         asm volatile("s_waitcnt lgkmcnt(0)" ::: "memory");
;         float rli[16];
; #pragma unroll
;         for (int r = 0; r < 16; ++r) rli[r] = __builtin_amdgcn_rcpf(li_l[crow(r, hf)]);
;         store_o_bf16(o, rli, Ob, RSTR * 3072, lane, r32, hf);
.LBB0_1017:
	s_or_b64 exec, exec, s[6:7]
	s_waitcnt lgkmcnt(0)
	ds_read_b128 v[66:69], v200
	ds_read_b128 v[70:73], v200 offset:32
	s_waitcnt vmcnt(15)
	v_and_b32_e32 v84, 1, v194
	v_cmp_eq_u32_e32 vcc, 0, v84
	v_or_b32_e32 v0, v202, v84
	s_waitcnt lgkmcnt(1)
	v_rcp_f32_e32 v74, v66
	v_rcp_f32_e32 v75, v67
	v_mul_lo_u32 v0, v0, s70
	v_and_or_b32 v0, v194, 30, v0
	v_mul_f32_e32 v50, v50, v74
	v_mul_f32_e32 v51, v51, v75
	v_cndmask_b32_e32 v84, v50, v51, vcc
	v_rcp_f32_e32 v76, v68
	v_rcp_f32_e32 v77, v69
	v_mov_b32_dpp v84, v84 quad_perm:[1,0,3,2] row_mask:0xf bank_mask:0xf bound_ctrl:1
	v_cndmask_b32_e32 v50, v84, v50, vcc
	s_waitcnt lgkmcnt(0)
	v_rcp_f32_e32 v78, v70
	ds_read_b128 v[66:69], v200 offset:64
	v_rcp_f32_e32 v79, v71
	v_rcp_f32_e32 v80, v72
	v_rcp_f32_e32 v81, v73
	ds_read_b128 v[70:73], v200 offset:96
	v_lshlrev_b32_e32 v0, 1, v0
	v_cndmask_b32_e32 v51, v51, v84, vcc
	v_cvt_pk_bf16_f32 v50, v50, v51
	v_mul_f32_e32 v34, v34, v74
	v_mul_f32_e32 v35, v35, v75
	v_lshrrev_b32_e32 v100, 4, v194
	v_mul_u32_u24_e32 v100, 0x18000, v100
	v_and_b32_e32 v101, 15, v194
	v_lshl_add_u32 v100, v101, 4, v100
	v_mov_b32_e32 v101, 0
	v_lshl_add_u64 v[100:101], s[16:17], 0, v[100:101]
	v_and_b32_e32 v98, 1, v194
	v_lshrrev_b32_e32 v99, 3, v194
	v_and_b32_e32 v99, 4, v99
	v_add_u32_e32 v98, v98, v99
	v_lshlrev_b32_e32 v98, 8, v98
	v_and_b32_e32 v99, 30, v194
	v_lshl_add_u32 v98, v99, 1, v98
	v_add_u32_e32 v98, s29, v98
	v_lshlrev_b32_e32 v99, 4, v194
	v_add_u32_e32 v99, s29, v99
	ds_write_b32 v98, v50 offset:0
	v_cndmask_b32_e32 v50, v34, v35, vcc
	v_mul_f32_e32 v18, v18, v74
	v_mul_f32_e32 v19, v19, v75
	v_mov_b32_dpp v50, v50 quad_perm:[1,0,3,2] row_mask:0xf bank_mask:0xf bound_ctrl:1
	v_cndmask_b32_e32 v34, v50, v34, vcc
	v_cndmask_b32_e32 v35, v35, v50, vcc
	v_cvt_pk_bf16_f32 v34, v34, v35
	ds_write_b32 v98, v34 offset:64
	v_cndmask_b32_e32 v34, v18, v19, vcc
	v_mul_f32_e32 v2, v2, v74
	v_mul_f32_e32 v3, v3, v75
	v_mov_b32_dpp v34, v34 quad_perm:[1,0,3,2] row_mask:0xf bank_mask:0xf bound_ctrl:1
	v_cndmask_b32_e32 v18, v34, v18, vcc
	v_cndmask_b32_e32 v19, v19, v34, vcc
	v_cvt_pk_bf16_f32 v18, v18, v19
	ds_write_b32 v98, v18 offset:128
	v_cndmask_b32_e32 v18, v2, v3, vcc
	s_waitcnt lgkmcnt(1)
	v_rcp_f32_e32 v82, v66
	v_rcp_f32_e32 v83, v67
	v_mov_b32_dpp v18, v18 quad_perm:[1,0,3,2] row_mask:0xf bank_mask:0xf bound_ctrl:1
	v_cndmask_b32_e32 v2, v18, v2, vcc
	v_cndmask_b32_e32 v3, v3, v18, vcc
	v_cvt_pk_bf16_f32 v2, v2, v3
	v_lshl_add_u64 v[66:67], s[16:17], 0, v[0:1]
	ds_write_b32 v98, v2 offset:192
	v_mul_f32_e32 v0, v52, v76
	v_mul_f32_e32 v2, v53, v77
	v_cndmask_b32_e32 v3, v0, v2, vcc
	v_mul_f32_e32 v18, v37, v77
	v_rcp_f32_e32 v68, v68
	v_mov_b32_dpp v3, v3 quad_perm:[1,0,3,2] row_mask:0xf bank_mask:0xf bound_ctrl:1
	v_cndmask_b32_e32 v0, v3, v0, vcc
	v_cndmask_b32_e32 v2, v2, v3, vcc
	v_cvt_pk_bf16_f32 v0, v0, v2
	v_add_co_u32_e64 v2, s[4:5], s58, v66
	v_rcp_f32_e32 v69, v69
	s_nop 0
	v_addc_co_u32_e64 v3, s[4:5], 0, v67, s[4:5]
	ds_write_b32 v98, v0 offset:512
	v_mul_f32_e32 v0, v36, v76
	v_cndmask_b32_e32 v19, v0, v18, vcc
	s_mov_b32 s4, 0xc0000
	s_waitcnt lgkmcnt(0)
	v_rcp_f32_e32 v70, v70
	v_mov_b32_dpp v19, v19 quad_perm:[1,0,3,2] row_mask:0xf bank_mask:0xf bound_ctrl:1
	v_cndmask_b32_e32 v0, v19, v0, vcc
	v_cndmask_b32_e32 v18, v18, v19, vcc
	v_cvt_pk_bf16_f32 v0, v0, v18
	ds_write_b32 v98, v0 offset:576
	v_mul_f32_e32 v0, v20, v76
	v_mul_f32_e32 v18, v21, v77
	v_cndmask_b32_e32 v19, v0, v18, vcc
	v_rcp_f32_e32 v71, v71
	v_rcp_f32_e32 v72, v72
	v_mov_b32_dpp v19, v19 quad_perm:[1,0,3,2] row_mask:0xf bank_mask:0xf bound_ctrl:1
	v_cndmask_b32_e32 v0, v19, v0, vcc
	v_cndmask_b32_e32 v18, v18, v19, vcc
	v_cvt_pk_bf16_f32 v0, v0, v18
	ds_write_b32 v98, v0 offset:640
	v_mul_f32_e32 v0, v4, v76
	v_mul_f32_e32 v4, v5, v77
	v_cndmask_b32_e32 v5, v0, v4, vcc
	v_rcp_f32_e32 v73, v73
	s_add_i32 s68, s68, s97
	v_mov_b32_dpp v5, v5 quad_perm:[1,0,3,2] row_mask:0xf bank_mask:0xf bound_ctrl:1
	v_cndmask_b32_e32 v0, v5, v0, vcc
	v_cndmask_b32_e32 v4, v4, v5, vcc
	v_cvt_pk_bf16_f32 v0, v0, v4
	ds_write_b32 v98, v0 offset:704
	v_mul_f32_e32 v0, v54, v78
	v_mul_f32_e32 v2, v55, v79
	v_cndmask_b32_e32 v3, v0, v2, vcc
	v_mul_f32_e32 v4, v39, v79
	s_cmpk_gt_i32 s68, 0x1ff
	v_mov_b32_dpp v3, v3 quad_perm:[1,0,3,2] row_mask:0xf bank_mask:0xf bound_ctrl:1
	v_cndmask_b32_e32 v0, v3, v0, vcc
	v_cndmask_b32_e32 v2, v2, v3, vcc
	v_cvt_pk_bf16_f32 v0, v0, v2
	v_add_co_u32_e64 v2, s[4:5], s4, v66
	s_mov_b64 s[86:87], s[52:53]
	s_nop 0
	v_addc_co_u32_e64 v3, s[4:5], 0, v67, s[4:5]
	ds_write_b32 v98, v0 offset:2048
	v_mul_f32_e32 v0, v38, v78
	v_cndmask_b32_e32 v5, v0, v4, vcc
	s_mov_b32 s83, s81
	s_movk_i32 s84, 0x2000
	v_mov_b32_dpp v5, v5 quad_perm:[1,0,3,2] row_mask:0xf bank_mask:0xf bound_ctrl:1
	v_cndmask_b32_e32 v0, v5, v0, vcc
	v_cndmask_b32_e32 v4, v4, v5, vcc
	v_cvt_pk_bf16_f32 v0, v0, v4
	ds_write_b32 v98, v0 offset:2112
	v_mul_f32_e32 v0, v22, v78
	v_mul_f32_e32 v4, v23, v79
	v_cndmask_b32_e32 v5, v0, v4, vcc
	s_nop 1
	v_mov_b32_dpp v5, v5 quad_perm:[1,0,3,2] row_mask:0xf bank_mask:0xf bound_ctrl:1
	v_cndmask_b32_e32 v0, v5, v0, vcc
	v_cndmask_b32_e32 v4, v4, v5, vcc
	v_cvt_pk_bf16_f32 v0, v0, v4
	ds_write_b32 v98, v0 offset:2176
	v_mul_f32_e32 v0, v6, v78
	v_mul_f32_e32 v4, v7, v79
	v_cndmask_b32_e32 v5, v0, v4, vcc
	s_nop 1
	v_mov_b32_dpp v5, v5 quad_perm:[1,0,3,2] row_mask:0xf bank_mask:0xf bound_ctrl:1
	v_cndmask_b32_e32 v0, v5, v0, vcc
	v_cndmask_b32_e32 v4, v4, v5, vcc
	v_cvt_pk_bf16_f32 v0, v0, v4
	ds_write_b32 v98, v0 offset:2240
	v_mul_f32_e32 v0, v56, v80
	v_mul_f32_e32 v2, v57, v81
	v_cndmask_b32_e32 v3, v0, v2, vcc
	v_mul_f32_e32 v4, v41, v81
; __device__ __forceinline__ float lane_xor1(float v) { return dpp_f<0xB1>(v); }
; __device__ __forceinline__ unsigned cvtpk(float lo, float hi) { unsigned r; asm volatile("v_cvt_pk_bf16_f32 %0, %1, %2" : "=v"(r) : "v"(lo), "v"(hi)); return r; }
; __device__ __forceinline__ void store_o_bf16(const f32x16* o, const float* rli, bf16* Ow, int ldo, int lane, int r32, int hi) {
;     ...
;   for (int r = 0; r < 16; r += 2) {
;     char* rowp = (char*)(Ow + (size_t)((r & 3) + 8 * (r >> 2)) * ldo);
; #pragma unroll
;     for (int d0 = 0; d0 < 4; ++d0) {
;       const float a = o[d0][r] * rli[r], b = o[d0][r + 1] * rli[r + 1];
;       const float send = (lane & 1) ? a : b; const float recv = lane_xor1(send);
;       const unsigned w = cvtpk((lane & 1) ? recv : a, (lane & 1) ? b : recv);
;       *(unsigned*)(rowp + loff + d0 * 64) = w; } }
	s_nop 0
	v_mov_b32_dpp v3, v3 quad_perm:[1,0,3,2] row_mask:0xf bank_mask:0xf bound_ctrl:1
	v_cndmask_b32_e32 v0, v3, v0, vcc
	v_cndmask_b32_e32 v2, v2, v3, vcc
	v_cvt_pk_bf16_f32 v0, v0, v2
	v_add_co_u32_e64 v2, s[4:5], s49, v66
	s_nop 1
	v_addc_co_u32_e64 v3, s[4:5], 0, v67, s[4:5]
	ds_write_b32 v98, v0 offset:2560
	v_mul_f32_e32 v0, v40, v80
	v_cndmask_b32_e32 v5, v0, v4, vcc
	s_mov_b32 s4, 0x180000
	s_nop 0
	v_mov_b32_dpp v5, v5 quad_perm:[1,0,3,2] row_mask:0xf bank_mask:0xf bound_ctrl:1
	v_cndmask_b32_e32 v0, v5, v0, vcc
	v_cndmask_b32_e32 v4, v4, v5, vcc
	v_cvt_pk_bf16_f32 v0, v0, v4
	ds_write_b32 v98, v0 offset:2624
	v_mul_f32_e32 v0, v24, v80
	v_mul_f32_e32 v4, v25, v81
	v_cndmask_b32_e32 v5, v0, v4, vcc
	s_nop 1
	v_mov_b32_dpp v5, v5 quad_perm:[1,0,3,2] row_mask:0xf bank_mask:0xf bound_ctrl:1
	v_cndmask_b32_e32 v0, v5, v0, vcc
	v_cndmask_b32_e32 v4, v4, v5, vcc
	v_cvt_pk_bf16_f32 v0, v0, v4
	ds_write_b32 v98, v0 offset:2688
	v_mul_f32_e32 v0, v8, v80
	v_mul_f32_e32 v4, v9, v81
	v_cndmask_b32_e32 v5, v0, v4, vcc
	s_nop 1
	v_mov_b32_dpp v5, v5 quad_perm:[1,0,3,2] row_mask:0xf bank_mask:0xf bound_ctrl:1
	v_cndmask_b32_e32 v0, v5, v0, vcc
	v_cndmask_b32_e32 v4, v4, v5, vcc
	v_cvt_pk_bf16_f32 v0, v0, v4
	ds_write_b32 v98, v0 offset:2752
	v_mul_f32_e32 v0, v58, v82
	v_mul_f32_e32 v2, v59, v83
	v_cndmask_b32_e32 v3, v0, v2, vcc
	v_mul_f32_e32 v4, v43, v83
	s_nop 0
	v_mov_b32_dpp v3, v3 quad_perm:[1,0,3,2] row_mask:0xf bank_mask:0xf bound_ctrl:1
	v_cndmask_b32_e32 v0, v3, v0, vcc
	v_cndmask_b32_e32 v2, v2, v3, vcc
	v_cvt_pk_bf16_f32 v0, v0, v2
	v_add_co_u32_e64 v2, s[4:5], s4, v66
	s_nop 1
	v_addc_co_u32_e64 v3, s[4:5], 0, v67, s[4:5]
	ds_write_b32 v98, v0 offset:4096
	v_mul_f32_e32 v0, v42, v82
	v_cndmask_b32_e32 v5, v0, v4, vcc
	s_nop 1
	v_mov_b32_dpp v5, v5 quad_perm:[1,0,3,2] row_mask:0xf bank_mask:0xf bound_ctrl:1
	v_cndmask_b32_e32 v0, v5, v0, vcc
	v_cndmask_b32_e32 v4, v4, v5, vcc
	v_cvt_pk_bf16_f32 v0, v0, v4
	ds_write_b32 v98, v0 offset:4160
	v_mul_f32_e32 v0, v26, v82
	v_mul_f32_e32 v4, v27, v83
	v_cndmask_b32_e32 v5, v0, v4, vcc
	s_nop 1
	v_mov_b32_dpp v5, v5 quad_perm:[1,0,3,2] row_mask:0xf bank_mask:0xf bound_ctrl:1
	v_cndmask_b32_e32 v0, v5, v0, vcc
	v_cndmask_b32_e32 v4, v4, v5, vcc
	v_cvt_pk_bf16_f32 v0, v0, v4
	ds_write_b32 v98, v0 offset:4224
	v_mul_f32_e32 v0, v10, v82
	v_mul_f32_e32 v4, v11, v83
	v_cndmask_b32_e32 v5, v0, v4, vcc
	s_nop 1
	v_mov_b32_dpp v5, v5 quad_perm:[1,0,3,2] row_mask:0xf bank_mask:0xf bound_ctrl:1
	v_cndmask_b32_e32 v0, v5, v0, vcc
	v_cndmask_b32_e32 v4, v4, v5, vcc
	v_cvt_pk_bf16_f32 v0, v0, v4
	ds_write_b32 v98, v0 offset:4288
	v_mul_f32_e32 v0, v60, v68
	v_mul_f32_e32 v2, v61, v69
	v_cndmask_b32_e32 v3, v0, v2, vcc
	v_mul_f32_e32 v4, v45, v69
	s_nop 0
	v_mov_b32_dpp v3, v3 quad_perm:[1,0,3,2] row_mask:0xf bank_mask:0xf bound_ctrl:1
	v_cndmask_b32_e32 v0, v3, v0, vcc
	v_cndmask_b32_e32 v2, v2, v3, vcc
	v_cvt_pk_bf16_f32 v0, v0, v2
	v_add_co_u32_e64 v2, s[4:5], s59, v66
	s_nop 1
	v_addc_co_u32_e64 v3, s[4:5], 0, v67, s[4:5]
	ds_write_b32 v98, v0 offset:4608
	v_mul_f32_e32 v0, v44, v68
	v_cndmask_b32_e32 v5, v0, v4, vcc
	s_nop 1
	v_mov_b32_dpp v5, v5 quad_perm:[1,0,3,2] row_mask:0xf bank_mask:0xf bound_ctrl:1
	v_cndmask_b32_e32 v0, v5, v0, vcc
	v_cndmask_b32_e32 v4, v4, v5, vcc
	v_cvt_pk_bf16_f32 v0, v0, v4
	ds_write_b32 v98, v0 offset:4672
	v_mul_f32_e32 v0, v28, v68
	v_mul_f32_e32 v4, v29, v69
	v_cndmask_b32_e32 v5, v0, v4, vcc
	s_nop 1
	v_mov_b32_dpp v5, v5 quad_perm:[1,0,3,2] row_mask:0xf bank_mask:0xf bound_ctrl:1
	v_cndmask_b32_e32 v0, v5, v0, vcc
	v_cndmask_b32_e32 v4, v4, v5, vcc
	v_cvt_pk_bf16_f32 v0, v0, v4
	ds_write_b32 v98, v0 offset:4736
	v_mul_f32_e32 v0, v12, v68
	v_mul_f32_e32 v4, v13, v69
	v_cndmask_b32_e32 v5, v0, v4, vcc
	s_nop 1
	v_mov_b32_dpp v5, v5 quad_perm:[1,0,3,2] row_mask:0xf bank_mask:0xf bound_ctrl:1
	v_cndmask_b32_e32 v0, v5, v0, vcc
	v_cndmask_b32_e32 v4, v4, v5, vcc
	v_cvt_pk_bf16_f32 v0, v0, v4
	ds_write_b32 v98, v0 offset:4800
	v_mul_f32_e32 v0, v62, v70
	v_mul_f32_e32 v2, v63, v71
	v_cndmask_b32_e32 v3, v0, v2, vcc
	v_mul_f32_e32 v4, v47, v71
	s_nop 0
	v_mov_b32_dpp v3, v3 quad_perm:[1,0,3,2] row_mask:0xf bank_mask:0xf bound_ctrl:1
	v_cndmask_b32_e32 v0, v3, v0, vcc
	v_cndmask_b32_e32 v2, v2, v3, vcc
	v_cvt_pk_bf16_f32 v0, v0, v2
	v_add_co_u32_e64 v2, s[4:5], s96, v66
	s_nop 1
	v_addc_co_u32_e64 v3, s[4:5], 0, v67, s[4:5]
	ds_write_b32 v98, v0 offset:6144
	v_mul_f32_e32 v0, v46, v70
	v_cndmask_b32_e32 v5, v0, v4, vcc
	s_nop 1
	v_mov_b32_dpp v5, v5 quad_perm:[1,0,3,2] row_mask:0xf bank_mask:0xf bound_ctrl:1
	v_cndmask_b32_e32 v0, v5, v0, vcc
	v_cndmask_b32_e32 v4, v4, v5, vcc
	v_cvt_pk_bf16_f32 v0, v0, v4
	ds_write_b32 v98, v0 offset:6208
	v_mul_f32_e32 v0, v30, v70
	v_mul_f32_e32 v4, v31, v71
	v_cndmask_b32_e32 v5, v0, v4, vcc
	s_nop 1
	v_mov_b32_dpp v5, v5 quad_perm:[1,0,3,2] row_mask:0xf bank_mask:0xf bound_ctrl:1
	v_cndmask_b32_e32 v0, v5, v0, vcc
	v_cndmask_b32_e32 v4, v4, v5, vcc
	v_cvt_pk_bf16_f32 v0, v0, v4
	ds_write_b32 v98, v0 offset:6272
	v_mul_f32_e32 v0, v14, v70
	v_mul_f32_e32 v4, v15, v71
	v_cndmask_b32_e32 v5, v0, v4, vcc
	s_nop 1
	v_mov_b32_dpp v5, v5 quad_perm:[1,0,3,2] row_mask:0xf bank_mask:0xf bound_ctrl:1
	v_cndmask_b32_e32 v0, v5, v0, vcc
	v_cndmask_b32_e32 v4, v4, v5, vcc
	v_cvt_pk_bf16_f32 v0, v0, v4
	ds_write_b32 v98, v0 offset:6336
	v_mul_f32_e32 v0, v64, v72
	v_mul_f32_e32 v2, v65, v73
	v_cndmask_b32_e32 v3, v0, v2, vcc
	v_mul_f32_e32 v4, v49, v73
	s_nop 0
	v_mov_b32_dpp v3, v3 quad_perm:[1,0,3,2] row_mask:0xf bank_mask:0xf bound_ctrl:1
	v_cndmask_b32_e32 v0, v3, v0, vcc
	v_cndmask_b32_e32 v2, v2, v3, vcc
	v_cvt_pk_bf16_f32 v0, v0, v2
	v_add_co_u32_e64 v2, s[4:5], s75, v66
	s_nop 1
	v_addc_co_u32_e64 v3, s[4:5], 0, v67, s[4:5]
	ds_write_b32 v98, v0 offset:6656
	v_mul_f32_e32 v0, v48, v72
	v_cndmask_b32_e32 v5, v0, v4, vcc
	s_nop 1
	v_mov_b32_dpp v5, v5 quad_perm:[1,0,3,2] row_mask:0xf bank_mask:0xf bound_ctrl:1
	v_cndmask_b32_e32 v0, v5, v0, vcc
	v_cndmask_b32_e32 v4, v4, v5, vcc
	v_cvt_pk_bf16_f32 v0, v0, v4
	ds_write_b32 v98, v0 offset:6720
	v_mul_f32_e32 v0, v32, v72
	v_mul_f32_e32 v4, v33, v73
	v_cndmask_b32_e32 v5, v0, v4, vcc
	s_nop 1
	v_mov_b32_dpp v5, v5 quad_perm:[1,0,3,2] row_mask:0xf bank_mask:0xf bound_ctrl:1
	v_cndmask_b32_e32 v0, v5, v0, vcc
	v_cndmask_b32_e32 v4, v4, v5, vcc
	v_cvt_pk_bf16_f32 v0, v0, v4
	ds_write_b32 v98, v0 offset:6784
	v_mul_f32_e32 v0, v16, v72
	v_mul_f32_e32 v4, v17, v73
	v_cndmask_b32_e32 v5, v0, v4, vcc
	s_nop 1
	v_mov_b32_dpp v5, v5 quad_perm:[1,0,3,2] row_mask:0xf bank_mask:0xf bound_ctrl:1
	v_cndmask_b32_e32 v0, v5, v0, vcc
	v_cndmask_b32_e32 v4, v4, v5, vcc
	v_cvt_pk_bf16_f32 v0, v0, v4
	ds_write_b32 v98, v0 offset:6848
	ds_read_b128 v[236:239], v99 offset:0
	ds_read_b128 v[240:243], v99 offset:1024
	ds_read_b128 v[244:247], v99 offset:2048
	ds_read_b128 v[248:251], v99 offset:3072
	s_waitcnt lgkmcnt(3)
; __device__ __forceinline__ float lane_xor1(float v) { return dpp_f<0xB1>(v); }
; __device__ __forceinline__ unsigned cvtpk(float lo, float hi) { unsigned r; asm volatile("v_cvt_pk_bf16_f32 %0, %1, %2" : "=v"(r) : "v"(lo), "v"(hi)); return r; }
; __device__ __forceinline__ void store_o_bf16(const f32x16* o, const float* rli, bf16* Ow, int ldo, int lane, int r32, int hi) {
;     ...
;   for (int r = 0; r < 16; r += 2) {
;     char* rowp = (char*)(Ow + (size_t)((r & 3) + 8 * (r >> 2)) * ldo);
; #pragma unroll
;     for (int d0 = 0; d0 < 4; ++d0) {
;       const float a = o[d0][r] * rli[r], b = o[d0][r + 1] * rli[r + 1];
;       const float send = (lane & 1) ? a : b; const float recv = lane_xor1(send);
;       const unsigned w = cvtpk((lane & 1) ? recv : a, (lane & 1) ? b : recv);
;       *(unsigned*)(rowp + loff + d0 * 64) = w; } }
; template <int PASS>
; __device__ __forceinline__ void attn_a_pass(LAS unsigned char* lds_all, const bf16* ZA, bf16* Oabc, float* ML, const float* rel_bias, int gw, int ngw, int xcd, int inx, int tid) {
;     ...
;     for (int q = wih; q < 512; q += nwh) {
	global_store_dwordx4 v[100:101], v[236:239], off
	s_mov_b32 s94, 0x60000
	v_add_co_u32_e64 v102, s[98:99], s94, v100
	s_nop 1
	v_addc_co_u32_e64 v103, s[98:99], 0, v101, s[98:99]
	s_waitcnt lgkmcnt(2)
	global_store_dwordx4 v[102:103], v[240:243], off
	s_mov_b32 s94, 0xc0000
	v_add_co_u32_e64 v104, s[98:99], s94, v100
	s_nop 1
	v_addc_co_u32_e64 v105, s[98:99], 0, v101, s[98:99]
	s_waitcnt lgkmcnt(1)
	global_store_dwordx4 v[104:105], v[244:247], off
	s_mov_b32 s94, 0x120000
	v_add_co_u32_e64 v102, s[98:99], s94, v100
	s_nop 1
	v_addc_co_u32_e64 v103, s[98:99], 0, v101, s[98:99]
	s_waitcnt lgkmcnt(0)
	global_store_dwordx4 v[102:103], v[248:251], off
	ds_read_b128 v[204:207], v99 offset:4096
	ds_read_b128 v[208:211], v99 offset:5120
	ds_read_b128 v[212:215], v99 offset:6144
	ds_read_b128 v[110:113], v99 offset:7168
	s_mov_b32 s94, 0x180000
	v_add_co_u32_e64 v104, s[98:99], s94, v100
	s_nop 1
	v_addc_co_u32_e64 v105, s[98:99], 0, v101, s[98:99]
	s_waitcnt lgkmcnt(3)
	global_store_dwordx4 v[104:105], v[204:207], off
	s_mov_b32 s94, 0x1e0000
	v_add_co_u32_e64 v102, s[98:99], s94, v100
	s_nop 1
	v_addc_co_u32_e64 v103, s[98:99], 0, v101, s[98:99]
	s_waitcnt lgkmcnt(2)
	global_store_dwordx4 v[102:103], v[208:211], off
	s_mov_b32 s94, 0x240000
	v_add_co_u32_e64 v104, s[98:99], s94, v100
	s_nop 1
	v_addc_co_u32_e64 v105, s[98:99], 0, v101, s[98:99]
	s_waitcnt lgkmcnt(1)
	global_store_dwordx4 v[104:105], v[212:215], off
	s_mov_b32 s94, 0x2a0000
	v_add_co_u32_e64 v102, s[98:99], s94, v100
	s_nop 1
	v_addc_co_u32_e64 v103, s[98:99], 0, v101, s[98:99]
	s_waitcnt lgkmcnt(0)
	global_store_dwordx4 v[102:103], v[110:113], off
	s_cbranch_scc1 .LBB0_1007
